# down-GEMM epilogue: the 7 later Y-row addresses derived from the first by one 64-bit add of a scalar constant (28 fewer VALU per unit), on top of v141
# baseline (speedup 1.0000x reference)
.LBB0_2094:
.LBB0_2096:
	s_mov_b32 s33, 0
	v_mov_b32_e32 v2, v166
	v_mov_b32_e32 v3, v165
	v_mov_b32_e32 v4, s39
	ds_read_b32 v4, v4 offset:288
	s_lshl_b32 s15, s85, 11
	v_lshlrev_b32_e32 v18, 3, v2
	s_add_i32 s15, s15, 0
	s_add_i32 s15, s15, 0x21000
	v_add_u32_e32 v2, s66, v18
	v_lshl_add_u32 v8, v2, 2, s15
	ds_read_b128 v[10:13], v8
	s_waitcnt lgkmcnt(1)
	v_readfirstlane_b32 s17, v4
	s_lshl_b32 s17, s17, 2
	s_add_i32 s17, s17, 0
	s_add_i32 s17, s17, 0x201c0
	v_mov_b32_e32 v2, s17
	ds_read2_b32 v[6:7], v2 offset1:32
	v_add_u32_e32 v19, s29, v3
	v_add_u32_e32 v21, 16, v19
	v_add_u32_e32 v23, 32, v19
	v_lshl_add_u32 v22, v21, 2, s15
	s_waitcnt lgkmcnt(0)
	v_readfirstlane_b32 s17, v7
	s_sub_i32 s17, s22, s17
	v_readfirstlane_b32 s26, v6
	v_lshl_add_u32 v6, v19, 2, s15
	v_lshl_add_u32 v24, v23, 2, s15
	ds_read_b128 v[14:17], v8 offset:16
	ds_read_b128 v[2:5], v8 offset:512
	s_lshl_b32 s17, s17, 8
	ds_read_b32 v25, v6 offset:1024
	ds_read_b128 v[6:9], v8 offset:528
	ds_read_b32 v22, v22 offset:1024
	ds_read_b32 v24, v24 offset:1024
	v_add_u32_e32 v20, s17, v19
	v_cmp_gt_i32_e32 vcc, s26, v20
	v_add_u32_e32 v20, s17, v21
	v_add_u32_e32 v27, 0xa0, v19
	s_waitcnt lgkmcnt(3)
	v_cndmask_b32_e32 v176, 0, v25, vcc
	v_cmp_gt_i32_e32 vcc, s26, v20
	v_add_u32_e32 v20, s17, v23
	v_add_u32_e32 v29, 0xb0, v19
	s_waitcnt lgkmcnt(1)
	v_cndmask_b32_e32 v178, 0, v22, vcc
	v_cmp_gt_i32_e32 vcc, s26, v20
	v_add_u32_e32 v20, 48, v19
	v_add_u32_e32 v22, 0x80, v19
	s_waitcnt lgkmcnt(0)
	v_cndmask_b32_e32 v32, 0, v24, vcc
	v_add_u32_e32 v24, 0x90, v19
	v_lshl_add_u32 v21, v20, 2, s15
	v_add_u32_e32 v20, s17, v20
	v_lshl_add_u32 v23, v22, 2, s15
	v_lshl_add_u32 v25, v24, 2, s15
	v_lshl_add_u32 v26, v27, 2, s15
	v_lshl_add_u32 v28, v29, 2, s15
	ds_read_b32 v21, v21 offset:1024
	ds_read_b32 v23, v23 offset:1024
	ds_read_b32 v25, v25 offset:1024
	ds_read_b32 v31, v26 offset:1024
	ds_read_b32 v33, v28 offset:1024
	v_cmp_gt_i32_e32 vcc, s26, v20
	v_add_u32_e32 v20, s17, v22
	v_mul_f32_e32 v180, 0x3b800000, v176
	s_waitcnt lgkmcnt(4)
	v_cndmask_b32_e32 v30, 0, v21, vcc
	v_cmp_gt_i32_e32 vcc, s26, v20
	v_lshl_add_u32 v22, s22, 8, v19
	v_pk_mul_f32 v[158:159], v[158:159], v[180:181] op_sel_hi:[1,0]
	s_waitcnt lgkmcnt(3)
	v_cndmask_b32_e32 v28, 0, v23, vcc
	v_add_u32_e32 v20, s17, v24
	v_ashrrev_i32_e32 v23, 31, v22
	v_pk_fma_f32 v[158:159], v[10:11], v[176:177], v[158:159] op_sel_hi:[1,0,1]
	v_pk_mul_f32 v[154:155], v[154:155], v[180:181] op_sel_hi:[1,0]
	v_cmp_gt_i32_e32 vcc, s26, v20
	v_lshlrev_b64 v[182:183], 10, v[22:23]
	v_pk_fma_f32 v[154:155], v[14:15], v[176:177], v[154:155] op_sel_hi:[1,0,1]
	v_med3_f32 v21, v158, s83, v173
	v_med3_f32 v23, v159, s83, v173
	s_waitcnt lgkmcnt(2)
	v_cndmask_b32_e32 v26, 0, v25, vcc
	v_add_u32_e32 v20, s17, v27
	v_cvt_pk_fp8_f32 v158, v21, v23
	v_med3_f32 v25, v154, s83, v173
	v_med3_f32 v27, v155, s83, v173
	v_pk_mul_f32 v[160:161], v[160:161], v[180:181] op_sel_hi:[1,0]
	v_cvt_pk_fp8_f32 v159, v25, v27
	v_pk_fma_f32 v[160:161], v[12:13], v[176:177], v[160:161] op_sel_hi:[1,0,1]
	v_pk_mul_f32 v[156:157], v[156:157], v[180:181] op_sel_hi:[1,0]
	v_med3_f32 v21, v160, s83, v173
	v_pk_fma_f32 v[156:157], v[16:17], v[176:177], v[156:157] op_sel_hi:[1,0,1]
	v_med3_f32 v23, v161, s83, v173
	v_pk_mul_f32 v[150:151], v[150:151], v[180:181] op_sel_hi:[1,0]
	v_cvt_pk_fp8_f32 v158, v21, v23 op_sel:[0,0,1]
	v_med3_f32 v21, v156, s83, v173
	v_med3_f32 v23, v157, s83, v173
	v_pk_fma_f32 v[150:151], v[2:3], v[176:177], v[150:151] op_sel_hi:[1,0,1]
	v_pk_mul_f32 v[146:147], v[146:147], v[180:181] op_sel_hi:[1,0]
	v_cvt_pk_fp8_f32 v159, v21, v23 op_sel:[0,0,1]
	v_pk_fma_f32 v[146:147], v[6:7], v[176:177], v[146:147] op_sel_hi:[1,0,1]
	v_med3_f32 v21, v150, s83, v173
	v_med3_f32 v23, v151, s83, v173
	v_cvt_pk_fp8_f32 v150, v21, v23
	v_med3_f32 v25, v146, s83, v173
	v_med3_f32 v27, v147, s83, v173
	v_pk_mul_f32 v[152:153], v[152:153], v[180:181] op_sel_hi:[1,0]
	v_cvt_pk_fp8_f32 v151, v25, v27
	v_pk_fma_f32 v[152:153], v[4:5], v[176:177], v[152:153] op_sel_hi:[1,0,1]
	v_pk_mul_f32 v[148:149], v[148:149], v[180:181] op_sel_hi:[1,0]
	v_med3_f32 v21, v152, s83, v173
	v_pk_fma_f32 v[148:149], v[8:9], v[176:177], v[148:149] op_sel_hi:[1,0,1]
	v_med3_f32 v23, v153, s83, v173
	s_or_b32 s27, s38, s66
	v_cvt_pk_fp8_f32 v150, v21, v23 op_sel:[0,0,1]
	v_med3_f32 v21, v148, s83, v173
	v_med3_f32 v23, v149, s83, v173
	v_add_u32_e32 v18, s27, v18
	v_cvt_pk_fp8_f32 v151, v21, v23 op_sel:[0,0,1]
	v_ashrrev_i32_e32 v19, 31, v18
	v_lshl_add_u64 v[146:147], s[10:11], 0, v[182:183]
	v_lshl_add_u64 v[184:185], v[146:147], 0, v[18:19]
	global_store_dwordx2 v[184:185], v[158:159], off
	global_store_dwordx2 v[184:185], v[150:151], off offset:128
	v_mul_f32_e32 v146, 0x3b800000, v178
	v_pk_mul_f32 v[142:143], v[142:143], v[146:147] op_sel_hi:[1,0]
	v_pk_mul_f32 v[138:139], v[138:139], v[146:147] op_sel_hi:[1,0]
	v_pk_fma_f32 v[142:143], v[10:11], v[178:179], v[142:143] op_sel_hi:[1,0,1]
	v_pk_fma_f32 v[138:139], v[14:15], v[178:179], v[138:139] op_sel_hi:[1,0,1]
	v_med3_f32 v21, v142, s83, v173
	v_med3_f32 v23, v143, s83, v173
	v_cvt_pk_fp8_f32 v142, v21, v23
	v_med3_f32 v25, v138, s83, v173
	v_med3_f32 v27, v139, s83, v173
	v_pk_mul_f32 v[144:145], v[144:145], v[146:147] op_sel_hi:[1,0]
	v_cvt_pk_fp8_f32 v143, v25, v27
	v_pk_fma_f32 v[144:145], v[12:13], v[178:179], v[144:145] op_sel_hi:[1,0,1]
	v_pk_mul_f32 v[140:141], v[140:141], v[146:147] op_sel_hi:[1,0]
	v_med3_f32 v21, v144, s83, v173
	v_pk_fma_f32 v[140:141], v[16:17], v[178:179], v[140:141] op_sel_hi:[1,0,1]
	v_med3_f32 v23, v145, s83, v173
	v_pk_mul_f32 v[134:135], v[134:135], v[146:147] op_sel_hi:[1,0]
	v_cvt_pk_fp8_f32 v142, v21, v23 op_sel:[0,0,1]
	v_med3_f32 v21, v140, s83, v173
	v_med3_f32 v23, v141, s83, v173
	v_pk_fma_f32 v[134:135], v[2:3], v[178:179], v[134:135] op_sel_hi:[1,0,1]
	v_pk_mul_f32 v[130:131], v[130:131], v[146:147] op_sel_hi:[1,0]
	v_cvt_pk_fp8_f32 v143, v21, v23 op_sel:[0,0,1]
	v_pk_fma_f32 v[130:131], v[6:7], v[178:179], v[130:131] op_sel_hi:[1,0,1]
	v_med3_f32 v21, v134, s83, v173
	v_med3_f32 v23, v135, s83, v173
	v_cvt_pk_fp8_f32 v134, v21, v23
	v_med3_f32 v25, v130, s83, v173
	v_med3_f32 v27, v131, s83, v173
	v_pk_mul_f32 v[136:137], v[136:137], v[146:147] op_sel_hi:[1,0]
	v_cvt_pk_fp8_f32 v135, v25, v27
	v_pk_fma_f32 v[136:137], v[4:5], v[178:179], v[136:137] op_sel_hi:[1,0,1]
	v_pk_mul_f32 v[132:133], v[132:133], v[146:147] op_sel_hi:[1,0]
	v_pk_fma_f32 v[132:133], v[8:9], v[178:179], v[132:133] op_sel_hi:[1,0,1]
	v_med3_f32 v21, v136, s83, v173
	v_med3_f32 v23, v137, s83, v173
	v_cvt_pk_fp8_f32 v134, v21, v23 op_sel:[0,0,1]
	v_med3_f32 v21, v132, s83, v173
	v_med3_f32 v23, v133, s83, v173
	v_cvt_pk_fp8_f32 v135, v21, v23 op_sel:[0,0,1]
	s_mov_b32 s32, 0x4000
	v_lshl_add_u64 v[130:131], v[184:185], 0, s[32:33]
	global_store_dwordx2 v[130:131], v[142:143], off
	global_store_dwordx2 v[130:131], v[134:135], off offset:128
	v_mul_f32_e32 v130, 0x3b800000, v32
	v_pk_mul_f32 v[126:127], v[126:127], v[130:131] op_sel_hi:[1,0]
	v_pk_mul_f32 v[122:123], v[122:123], v[130:131] op_sel_hi:[1,0]
	s_waitcnt lgkmcnt(0)
	v_pk_fma_f32 v[126:127], v[10:11], v[32:33], v[126:127] op_sel_hi:[1,0,1]
	v_pk_fma_f32 v[122:123], v[14:15], v[32:33], v[122:123] op_sel_hi:[1,0,1]
	v_med3_f32 v21, v126, s83, v173
	v_med3_f32 v23, v127, s83, v173
	v_cvt_pk_fp8_f32 v126, v21, v23
	v_med3_f32 v25, v122, s83, v173
	v_med3_f32 v27, v123, s83, v173
	v_pk_mul_f32 v[128:129], v[128:129], v[130:131] op_sel_hi:[1,0]
	v_cvt_pk_fp8_f32 v127, v25, v27
	v_pk_fma_f32 v[128:129], v[12:13], v[32:33], v[128:129] op_sel_hi:[1,0,1]
	v_pk_mul_f32 v[124:125], v[124:125], v[130:131] op_sel_hi:[1,0]
	v_cmp_gt_i32_e32 vcc, s26, v20
	v_add_u32_e32 v20, s17, v29
	v_pk_fma_f32 v[124:125], v[16:17], v[32:33], v[124:125] op_sel_hi:[1,0,1]
	v_med3_f32 v21, v128, s83, v173
	v_med3_f32 v23, v129, s83, v173
	v_pk_mul_f32 v[118:119], v[118:119], v[130:131] op_sel_hi:[1,0]
	v_cndmask_b32_e32 v24, 0, v31, vcc
	v_cmp_gt_i32_e32 vcc, s26, v20
	v_cvt_pk_fp8_f32 v126, v21, v23 op_sel:[0,0,1]
	v_med3_f32 v21, v124, s83, v173
	v_med3_f32 v23, v125, s83, v173
	v_pk_mul_f32 v[120:121], v[120:121], v[130:131] op_sel_hi:[1,0]
	v_pk_fma_f32 v[118:119], v[2:3], v[32:33], v[118:119] op_sel_hi:[1,0,1]
	v_pk_mul_f32 v[114:115], v[114:115], v[130:131] op_sel_hi:[1,0]
	v_pk_mul_f32 v[116:117], v[116:117], v[130:131] op_sel_hi:[1,0]
	v_cndmask_b32_e32 v20, 0, v33, vcc
	v_cvt_pk_fp8_f32 v127, v21, v23 op_sel:[0,0,1]
	v_pk_fma_f32 v[120:121], v[4:5], v[32:33], v[120:121] op_sel_hi:[1,0,1]
	v_pk_fma_f32 v[116:117], v[8:9], v[32:33], v[116:117] op_sel_hi:[1,0,1]
	v_pk_fma_f32 v[32:33], v[6:7], v[32:33], v[114:115] op_sel_hi:[1,0,1]
	v_med3_f32 v21, v118, s83, v173
	v_med3_f32 v23, v119, s83, v173
	v_cvt_pk_fp8_f32 v114, v21, v23
	v_med3_f32 v25, v32, s83, v173
	v_med3_f32 v27, v33, s83, v173
	v_cvt_pk_fp8_f32 v115, v25, v27
	v_med3_f32 v21, v120, s83, v173
	v_med3_f32 v23, v121, s83, v173
	v_cvt_pk_fp8_f32 v114, v21, v23 op_sel:[0,0,1]
	v_med3_f32 v21, v116, s83, v173
	v_med3_f32 v23, v117, s83, v173
	v_cvt_pk_fp8_f32 v115, v21, v23 op_sel:[0,0,1]
	s_mov_b32 s32, 0x8000
	v_lshl_add_u64 v[32:33], v[184:185], 0, s[32:33]
	global_store_dwordx2 v[32:33], v[126:127], off
	global_store_dwordx2 v[32:33], v[114:115], off offset:128
	v_mul_f32_e32 v32, 0x3b800000, v30
	v_pk_mul_f32 v[110:111], v[110:111], v[32:33] op_sel_hi:[1,0]
	v_pk_mul_f32 v[106:107], v[106:107], v[32:33] op_sel_hi:[1,0]
	v_pk_fma_f32 v[110:111], v[10:11], v[30:31], v[110:111] op_sel_hi:[1,0,1]
	v_pk_fma_f32 v[106:107], v[14:15], v[30:31], v[106:107] op_sel_hi:[1,0,1]
	v_med3_f32 v21, v110, s83, v173
	v_med3_f32 v23, v111, s83, v173
	v_cvt_pk_fp8_f32 v110, v21, v23
	v_med3_f32 v25, v106, s83, v173
	v_med3_f32 v27, v107, s83, v173
	v_pk_mul_f32 v[112:113], v[112:113], v[32:33] op_sel_hi:[1,0]
	v_cvt_pk_fp8_f32 v111, v25, v27
	v_pk_fma_f32 v[112:113], v[12:13], v[30:31], v[112:113] op_sel_hi:[1,0,1]
	v_pk_mul_f32 v[108:109], v[108:109], v[32:33] op_sel_hi:[1,0]
	v_med3_f32 v21, v112, s83, v173
	v_pk_fma_f32 v[108:109], v[16:17], v[30:31], v[108:109] op_sel_hi:[1,0,1]
	v_med3_f32 v23, v113, s83, v173
	v_pk_mul_f32 v[102:103], v[102:103], v[32:33] op_sel_hi:[1,0]
	v_cvt_pk_fp8_f32 v110, v21, v23 op_sel:[0,0,1]
	v_med3_f32 v21, v108, s83, v173
	v_med3_f32 v23, v109, s83, v173
	v_pk_mul_f32 v[104:105], v[104:105], v[32:33] op_sel_hi:[1,0]
	v_pk_fma_f32 v[102:103], v[2:3], v[30:31], v[102:103] op_sel_hi:[1,0,1]
	v_pk_mul_f32 v[98:99], v[98:99], v[32:33] op_sel_hi:[1,0]
	v_pk_mul_f32 v[32:33], v[100:101], v[32:33] op_sel_hi:[1,0]
	v_cvt_pk_fp8_f32 v111, v21, v23 op_sel:[0,0,1]
	v_pk_fma_f32 v[104:105], v[4:5], v[30:31], v[104:105] op_sel_hi:[1,0,1]
	v_pk_fma_f32 v[32:33], v[8:9], v[30:31], v[32:33] op_sel_hi:[1,0,1]
	v_pk_fma_f32 v[30:31], v[6:7], v[30:31], v[98:99] op_sel_hi:[1,0,1]
	v_med3_f32 v21, v102, s83, v173
	v_med3_f32 v23, v103, s83, v173
	v_cvt_pk_fp8_f32 v98, v21, v23
	v_med3_f32 v25, v30, s83, v173
	v_med3_f32 v27, v31, s83, v173
	v_med3_f32 v21, v104, s83, v173
	v_med3_f32 v23, v105, s83, v173
	v_cvt_pk_fp8_f32 v99, v25, v27
	v_cvt_pk_fp8_f32 v98, v21, v23 op_sel:[0,0,1]
	v_med3_f32 v21, v32, s83, v173
	v_mul_f32_e32 v32, 0x3b800000, v28
	v_pk_mul_f32 v[94:95], v[94:95], v[32:33] op_sel_hi:[1,0]
	v_med3_f32 v23, v33, s83, v173
	v_pk_fma_f32 v[94:95], v[10:11], v[28:29], v[94:95] op_sel_hi:[1,0,1]
	v_pk_mul_f32 v[90:91], v[90:91], v[32:33] op_sel_hi:[1,0]
	v_cvt_pk_fp8_f32 v99, v21, v23 op_sel:[0,0,1]
	v_pk_fma_f32 v[90:91], v[14:15], v[28:29], v[90:91] op_sel_hi:[1,0,1]
	v_med3_f32 v21, v94, s83, v173
	v_med3_f32 v23, v95, s83, v173
	v_cvt_pk_fp8_f32 v94, v21, v23
	v_med3_f32 v25, v90, s83, v173
	v_med3_f32 v27, v91, s83, v173
	v_pk_mul_f32 v[96:97], v[96:97], v[32:33] op_sel_hi:[1,0]
	v_cvt_pk_fp8_f32 v95, v25, v27
	v_pk_fma_f32 v[96:97], v[12:13], v[28:29], v[96:97] op_sel_hi:[1,0,1]
	v_pk_mul_f32 v[92:93], v[92:93], v[32:33] op_sel_hi:[1,0]
	v_med3_f32 v21, v96, s83, v173
	v_pk_fma_f32 v[92:93], v[16:17], v[28:29], v[92:93] op_sel_hi:[1,0,1]
	v_med3_f32 v23, v97, s83, v173
	v_pk_mul_f32 v[86:87], v[86:87], v[32:33] op_sel_hi:[1,0]
	v_cvt_pk_fp8_f32 v94, v21, v23 op_sel:[0,0,1]
	v_med3_f32 v21, v92, s83, v173
	v_med3_f32 v23, v93, s83, v173
	v_pk_mul_f32 v[88:89], v[88:89], v[32:33] op_sel_hi:[1,0]
	v_pk_fma_f32 v[86:87], v[2:3], v[28:29], v[86:87] op_sel_hi:[1,0,1]
	v_pk_mul_f32 v[82:83], v[82:83], v[32:33] op_sel_hi:[1,0]
	v_pk_mul_f32 v[32:33], v[84:85], v[32:33] op_sel_hi:[1,0]
	v_cvt_pk_fp8_f32 v95, v21, v23 op_sel:[0,0,1]
	v_pk_fma_f32 v[88:89], v[4:5], v[28:29], v[88:89] op_sel_hi:[1,0,1]
	v_pk_fma_f32 v[32:33], v[8:9], v[28:29], v[32:33] op_sel_hi:[1,0,1]
	v_pk_fma_f32 v[28:29], v[6:7], v[28:29], v[82:83] op_sel_hi:[1,0,1]
	v_med3_f32 v21, v86, s83, v173
	v_med3_f32 v23, v87, s83, v173
	v_cvt_pk_fp8_f32 v82, v21, v23
	v_med3_f32 v25, v28, s83, v173
	v_med3_f32 v27, v29, s83, v173
	v_cvt_pk_fp8_f32 v83, v25, v27
	s_mov_b32 s32, 0xc000
	v_lshl_add_u64 v[30:31], v[184:185], 0, s[32:33]
	global_store_dwordx2 v[30:31], v[110:111], off
	global_store_dwordx2 v[30:31], v[98:99], off offset:128
	v_med3_f32 v21, v88, s83, v173
	v_med3_f32 v23, v89, s83, v173
	v_cvt_pk_fp8_f32 v82, v21, v23 op_sel:[0,0,1]
	v_med3_f32 v21, v32, s83, v173
	v_med3_f32 v23, v33, s83, v173
	v_cvt_pk_fp8_f32 v83, v21, v23 op_sel:[0,0,1]
	s_mov_b32 s32, 0x20000
	v_lshl_add_u64 v[28:29], v[184:185], 0, s[32:33]
	global_store_dwordx2 v[28:29], v[94:95], off
	global_store_dwordx2 v[28:29], v[82:83], off offset:128
	v_mul_f32_e32 v28, 0x3b800000, v26
	v_pk_mul_f32 v[32:33], v[78:79], v[28:29] op_sel_hi:[1,0]
	v_pk_mul_f32 v[74:75], v[74:75], v[28:29] op_sel_hi:[1,0]
	v_pk_fma_f32 v[32:33], v[10:11], v[26:27], v[32:33] op_sel_hi:[1,0,1]
	v_pk_mul_f32 v[78:79], v[80:81], v[28:29] op_sel_hi:[1,0]
	v_pk_mul_f32 v[76:77], v[76:77], v[28:29] op_sel_hi:[1,0]
	v_pk_fma_f32 v[74:75], v[14:15], v[26:27], v[74:75] op_sel_hi:[1,0,1]
	v_med3_f32 v21, v32, s83, v173
	v_med3_f32 v23, v33, s83, v173
	v_pk_fma_f32 v[78:79], v[12:13], v[26:27], v[78:79] op_sel_hi:[1,0,1]
	v_pk_fma_f32 v[76:77], v[16:17], v[26:27], v[76:77] op_sel_hi:[1,0,1]
	v_cvt_pk_fp8_f32 v32, v21, v23
	v_med3_f32 v25, v74, s83, v173
	v_med3_f32 v27, v75, s83, v173
	v_cvt_pk_fp8_f32 v33, v25, v27
	v_med3_f32 v21, v78, s83, v173
	v_med3_f32 v23, v79, s83, v173
	v_pk_mul_f32 v[70:71], v[70:71], v[28:29] op_sel_hi:[1,0]
	v_cvt_pk_fp8_f32 v32, v21, v23 op_sel:[0,0,1]
	v_med3_f32 v21, v76, s83, v173
	v_med3_f32 v23, v77, s83, v173
	v_pk_mul_f32 v[72:73], v[72:73], v[28:29] op_sel_hi:[1,0]
	v_pk_fma_f32 v[70:71], v[2:3], v[26:27], v[70:71] op_sel_hi:[1,0,1]
	v_pk_mul_f32 v[66:67], v[66:67], v[28:29] op_sel_hi:[1,0]
	v_pk_mul_f32 v[28:29], v[68:69], v[28:29] op_sel_hi:[1,0]
	v_cvt_pk_fp8_f32 v33, v21, v23 op_sel:[0,0,1]
	v_pk_fma_f32 v[72:73], v[4:5], v[26:27], v[72:73] op_sel_hi:[1,0,1]
	v_pk_fma_f32 v[28:29], v[8:9], v[26:27], v[28:29] op_sel_hi:[1,0,1]
	v_pk_fma_f32 v[26:27], v[6:7], v[26:27], v[66:67] op_sel_hi:[1,0,1]
	v_med3_f32 v21, v70, s83, v173
	v_med3_f32 v23, v71, s83, v173
	v_cvt_pk_fp8_f32 v66, v21, v23
	v_med3_f32 v25, v26, s83, v173
	v_med3_f32 v26, v27, s83, v173
	v_cvt_pk_fp8_f32 v67, v25, v26
	v_med3_f32 v21, v72, s83, v173
	v_med3_f32 v23, v73, s83, v173
	v_cvt_pk_fp8_f32 v66, v21, v23 op_sel:[0,0,1]
	v_med3_f32 v21, v28, s83, v173
	v_med3_f32 v23, v29, s83, v173
	v_cvt_pk_fp8_f32 v67, v21, v23 op_sel:[0,0,1]
	s_mov_b32 s32, 0x24000
	v_lshl_add_u64 v[26:27], v[184:185], 0, s[32:33]
	global_store_dwordx2 v[26:27], v[32:33], off
	global_store_dwordx2 v[26:27], v[66:67], off offset:128
	v_mul_f32_e32 v26, 0x3b800000, v24
	v_pk_mul_f32 v[30:31], v[62:63], v[26:27] op_sel_hi:[1,0]
	v_pk_mul_f32 v[58:59], v[58:59], v[26:27] op_sel_hi:[1,0]
	v_pk_fma_f32 v[30:31], v[10:11], v[24:25], v[30:31] op_sel_hi:[1,0,1]
	v_pk_mul_f32 v[32:33], v[64:65], v[26:27] op_sel_hi:[1,0]
	v_pk_mul_f32 v[60:61], v[60:61], v[26:27] op_sel_hi:[1,0]
	v_pk_fma_f32 v[58:59], v[14:15], v[24:25], v[58:59] op_sel_hi:[1,0,1]
	v_med3_f32 v21, v30, s83, v173
	v_med3_f32 v23, v31, s83, v173
	v_pk_fma_f32 v[32:33], v[12:13], v[24:25], v[32:33] op_sel_hi:[1,0,1]
	v_pk_fma_f32 v[60:61], v[16:17], v[24:25], v[60:61] op_sel_hi:[1,0,1]
	v_cvt_pk_fp8_f32 v30, v21, v23
	v_med3_f32 v25, v58, s83, v173
	v_med3_f32 v27, v59, s83, v173
	v_cvt_pk_fp8_f32 v31, v25, v27
	v_med3_f32 v21, v32, s83, v173
	v_med3_f32 v23, v33, s83, v173
	v_pk_mul_f32 v[32:33], v[54:55], v[26:27] op_sel_hi:[1,0]
	v_cvt_pk_fp8_f32 v30, v21, v23 op_sel:[0,0,1]
	v_med3_f32 v21, v60, s83, v173
	v_med3_f32 v23, v61, s83, v173
	v_pk_mul_f32 v[54:55], v[56:57], v[26:27] op_sel_hi:[1,0]
	v_pk_fma_f32 v[32:33], v[2:3], v[24:25], v[32:33] op_sel_hi:[1,0,1]
	v_pk_mul_f32 v[50:51], v[50:51], v[26:27] op_sel_hi:[1,0]
	v_pk_mul_f32 v[26:27], v[52:53], v[26:27] op_sel_hi:[1,0]
	v_cvt_pk_fp8_f32 v31, v21, v23 op_sel:[0,0,1]
	v_pk_fma_f32 v[54:55], v[4:5], v[24:25], v[54:55] op_sel_hi:[1,0,1]
	v_pk_fma_f32 v[26:27], v[8:9], v[24:25], v[26:27] op_sel_hi:[1,0,1]
	v_pk_fma_f32 v[24:25], v[6:7], v[24:25], v[50:51] op_sel_hi:[1,0,1]
	v_med3_f32 v21, v32, s83, v173
	v_med3_f32 v23, v33, s83, v173
	v_cvt_pk_fp8_f32 v32, v21, v23
	v_med3_f32 v24, v24, s83, v173
	v_med3_f32 v25, v25, s83, v173
	v_cvt_pk_fp8_f32 v33, v24, v25
	v_med3_f32 v21, v54, s83, v173
	v_med3_f32 v23, v55, s83, v173
	v_cvt_pk_fp8_f32 v32, v21, v23 op_sel:[0,0,1]
	v_med3_f32 v21, v26, s83, v173
	v_med3_f32 v23, v27, s83, v173
	v_cvt_pk_fp8_f32 v33, v21, v23 op_sel:[0,0,1]
	s_mov_b32 s32, 0x28000
	v_lshl_add_u64 v[24:25], v[184:185], 0, s[32:33]
	global_store_dwordx2 v[24:25], v[30:31], off
	global_store_dwordx2 v[24:25], v[32:33], off offset:128
	v_mul_f32_e32 v24, 0x3b800000, v20
	v_pk_mul_f32 v[26:27], v[46:47], v[24:25] op_sel_hi:[1,0]
	v_pk_mul_f32 v[28:29], v[48:49], v[24:25] op_sel_hi:[1,0]
	v_pk_fma_f32 v[10:11], v[10:11], v[20:21], v[26:27] op_sel_hi:[1,0,1]
	v_pk_fma_f32 v[12:13], v[12:13], v[20:21], v[28:29] op_sel_hi:[1,0,1]
	v_pk_mul_f32 v[26:27], v[42:43], v[24:25] op_sel_hi:[1,0]
	v_pk_mul_f32 v[28:29], v[44:45], v[24:25] op_sel_hi:[1,0]
	v_pk_fma_f32 v[14:15], v[14:15], v[20:21], v[26:27] op_sel_hi:[1,0,1]
	v_pk_fma_f32 v[16:17], v[16:17], v[20:21], v[28:29] op_sel_hi:[1,0,1]
	v_med3_f32 v21, v10, s83, v173
	v_med3_f32 v11, v11, s83, v173
	v_cvt_pk_fp8_f32 v10, v21, v11
	v_med3_f32 v14, v14, s83, v173
	v_med3_f32 v15, v15, s83, v173
	v_cvt_pk_fp8_f32 v11, v14, v15
	v_med3_f32 v12, v12, s83, v173
	v_med3_f32 v13, v13, s83, v173
	v_cvt_pk_fp8_f32 v10, v12, v13 op_sel:[0,0,1]
	v_med3_f32 v12, v16, s83, v173
	v_med3_f32 v13, v17, s83, v173
	v_cvt_pk_fp8_f32 v11, v12, v13 op_sel:[0,0,1]
	v_pk_mul_f32 v[12:13], v[38:39], v[24:25] op_sel_hi:[1,0]
	v_pk_mul_f32 v[14:15], v[40:41], v[24:25] op_sel_hi:[1,0]
	v_pk_fma_f32 v[2:3], v[2:3], v[20:21], v[12:13] op_sel_hi:[1,0,1]
	v_pk_mul_f32 v[12:13], v[34:35], v[24:25] op_sel_hi:[1,0]
	v_med3_f32 v3, v3, s83, v173
	v_pk_fma_f32 v[6:7], v[6:7], v[20:21], v[12:13] op_sel_hi:[1,0,1]
	v_med3_f32 v12, v2, s83, v173
	v_mov_b32_e32 v2, 0
	v_cvt_pk_fp8_f32 v2, v12, v3
	v_med3_f32 v6, v6, s83, v173
	v_med3_f32 v7, v7, s83, v173
	v_cvt_pk_fp8_f32 v3, v6, v7
	v_pk_fma_f32 v[4:5], v[4:5], v[20:21], v[14:15] op_sel_hi:[1,0,1]
	v_pk_mul_f32 v[14:15], v[36:37], v[24:25] op_sel_hi:[1,0]
	v_pk_fma_f32 v[8:9], v[8:9], v[20:21], v[14:15] op_sel_hi:[1,0,1]
	v_med3_f32 v4, v4, s83, v173
	v_med3_f32 v5, v5, s83, v173
	v_cvt_pk_fp8_f32 v2, v4, v5 op_sel:[0,0,1]
	v_med3_f32 v4, v8, s83, v173
	v_med3_f32 v5, v9, s83, v173
	v_cvt_pk_fp8_f32 v3, v4, v5 op_sel:[0,0,1]
	s_mov_b32 s32, 0x2c000
	v_lshl_add_u64 v[4:5], v[184:185], 0, s[32:33]
	s_and_b64 vcc, exec, s[6:7]
	s_mov_b64 s[6:7], -1
	v_readlane_b32 s90, v253, 26
	global_store_dwordx2 v[4:5], v[10:11], off
	global_store_dwordx2 v[4:5], v[2:3], off offset:128
	s_cbranch_vccnz .LBB0_2057
	s_andn2_b64 vcc, exec, s[8:9]
	s_cbranch_vccnz .LBB0_2056
	s_barrier
	s_branch .LBB0_2056
